# sliding-window unit: sink-term positions requested in the prologue only (ticket still collected before the epilogue)
# speedup vs baseline: 1.0051x; 1.0051x over previous
; __device__ __forceinline__ int lane_id() { unsigned m = ~0u; asm volatile("" : "+s"(m)); return (int)__builtin_amdgcn_mbcnt_hi(m, __builtin_amdgcn_mbcnt_lo(m, 0u)); }
;     ...
;     const int tid = wv * 64 + lane, r32 = lane & 31, hf = lane >> 5;
;     const int wq = (MODE == 3) ? (wv & 3) : (MODE == 4) ? (wv & 1) : wv, mp = (MODE == 3) ? (wv >> 2) : 0, hsel = (MODE == 4) ? (wv >> 1) : 0;
;     if (MODE == 4) { slope_l2 = slp[hsel] * LOG2E; sink_l2 = snk[hsel] * LOG2E; }
;     const int qmin = q0 + 32 * wq, qidx = qmin + r32, qmax = qmin + 31;
;     int t_lo = 0; if (SWA) { t_lo = q0 - 127; t_lo = (t_lo < 0 ? 0 : t_lo) >> 7; }
;     const int t_hi = (q0 + ((MODE == 3) ? 127 : (MODE == 4) ? 63 : 255)) >> 7;
;     if (MODE == 3 && mp) kmax = kmax1;
;     const int pos_ref = ALIBI ? pos[q0] : 0;
;     bf16x8 qf[NC];
;     { const bf16_t* qr = T.q + (size_t)qidx * T.qp + 8 * hf + (mp + hsel) * DQK;
; #pragma unroll
;       for (int c = 0; c < NC; ++c) qf[c] = *(const bf16x8*)(qr + 16 * c); }
;     f32x16 ot[2];
; #pragma unroll
;     for (int i = 0; i < 16; ++i) { ot[0][i] = 0.f; ot[1][i] = 0.f; }
;     float m = SWA ? -1e30f : 0.f, l = 0.f; bool first = true;
;     u32x4 kreg[NKI], vreg[2]; float breg = 0.f;
;     const int vr = tid >> 3, vc = tid & 7;
;     ...
;     if (qmask & 8) for (;;) {
;         const int idx = at::claim_take(lds, F.tid, &pend); if (idx >= 512) break;
;         const int qb = idx >> 2, r = idx & 3, b = r >> 1, hk = r & 1;
;         const bf16_t* Hb = H + (size_t)b * S * HP;
;         at::Tens T{Hb + C_SWQ + hk * 256, Hb + C_SWKV + hk * 64, Hb + C_SWKV + 128 + hk * 64, HP, HP, HP};
;         at::softmax_unit<64, true, 4, false>(lds, wv, lane_id(), T, pos, qb * 64, 0.f, 0.f, O + (size_t)b * S * OP + 512 + hk * 256, OP, 0.f, nullptr, 0.f, 0.f, nullptr, q2ctr, &pend, slopes8 + 4 * hk, sinks + 4 * hk);
.LBB0_1027:
	s_and_saveexec_b64 s[16:17], s[38:39]
	ds_write_b32 v247, v164
	s_or_b64 exec, exec, s[16:17]
	s_waitcnt lgkmcnt(0)
	s_barrier
	ds_read_b32 v0, v247
	s_waitcnt lgkmcnt(0)
	s_barrier
	s_waitcnt lgkmcnt(0)
	v_readfirstlane_b32 s20, v0
	s_cmpk_gt_i32 s20, 0x1ff
	s_cselect_b64 s[16:17], -1, 0
	s_and_b64 vcc, exec, s[16:17]
	s_cbranch_vccnz .LBB0_1026
	s_lshl_b32 s3, s20, 12
	s_and_b32 s62, s3, 0x2000
	s_and_b32 s21, s20, 1
	s_mul_i32 s3, s62, 0x1600
	s_add_u32 s3, s2, s3
	s_addc_u32 s4, s1, 0
	s_lshl_b32 s28, s21, 9
	s_add_u32 s28, s3, s28
	s_addc_u32 s29, s4, 0
	s_lshl_b32 s40, s21, 7
	s_add_u32 s42, s3, s40
	s_mov_b32 s3, -1
	s_addc_u32 s43, s4, 0
	v_mbcnt_lo_u32_b32 v0, s3, 0
	v_mbcnt_hi_u32_b32 v4, s3, v0
	s_lshl_b32 s3, s20, 4
	s_and_b32 s40, s3, 0xffffffc0
	s_lshl_b32 s3, s21, 4
	v_mov_b32_e32 v0, s3
	v_readlane_b32 s3, v254, 18
	v_and_b32_e32 v5, 31, v4
	s_or_b32 s63, s40, s3
	v_ashrrev_i32_e32 v6, 5, v4
	global_load_dword v7, v0, s[10:11]
	global_load_dword v114, v0, s[34:35]
	v_or_b32_e32 v112, s63, v5
	s_max_i32 s3, s40, 0x7f
	s_ashr_i32 s41, s40, 31
	v_mov_b64_e32 v[0:1], s[28:29]
	s_addk_i32 s3, 0xff81
	s_lshl_b64 s[40:41], s[40:41], 2
	v_mad_i64_i32 v[0:1], s[28:29], v112, s33, v[0:1]
	v_lshlrev_b32_e32 v2, 3, v6
	s_add_u32 s40, s6, s40
	v_ashrrev_i32_e32 v3, 31, v2
	v_readlane_b32 s4, v254, 19
	v_readlane_b32 s28, v254, 53
	s_addc_u32 s41, s7, s41
	v_lshl_add_u64 v[0:1], v[2:3], 1, v[0:1]
	s_lshl_b32 s4, s4, 1
	v_add_u32_e32 v118, s28, v4
	v_lshl_add_u64 v[0:1], v[0:1], 0, s[4:5]
	v_ashrrev_i32_e32 v119, 31, v118
	global_load_dword v115, v31, s[40:41]
	v_ashrrev_i32_e32 v195, 31, v112
	v_mov_b32_e32 v194, v112
	v_lshl_add_u64 v[194:195], v[194:195], 2, s[6:7]
	global_load_dword v194, v[194:195], off
	global_load_dwordx4 v[80:83], v[0:1], off offset:2368
	global_load_dwordx4 v[84:87], v[0:1], off offset:2400
	global_load_dwordx4 v[88:91], v[0:1], off offset:2432
	global_load_dwordx4 v[92:95], v[0:1], off offset:2464
	v_lshrrev_b32_e32 v0, 29, v119
	v_add_u32_e32 v0, v118, v0
	s_and_b32 s44, s3, 0xffffff80
	v_ashrrev_i32_e32 v8, 3, v0
	v_and_b32_e32 v0, -8, v0
	v_sub_u32_e32 v11, v118, v0
	v_add_u32_e32 v0, s44, v8
	v_mov_b64_e32 v[2:3], s[42:43]
	v_mad_i64_i32 v[12:13], s[28:29], v0, s33, v[2:3]
	v_lshlrev_b32_e32 v0, 3, v11
	v_ashrrev_i32_e32 v1, 31, v0
	v_lshl_add_u64 v[14:15], v[0:1], 1, v[12:13]
	v_add_u32_e32 v12, 0x200, v118
	v_ashrrev_i32_e32 v9, 31, v12
	v_lshrrev_b32_e32 v9, 29, v9
	v_add_u32_e32 v13, v12, v9
	v_ashrrev_i32_e32 v9, 3, v13
	v_and_b32_e32 v13, -8, v13
	v_and_b32_e32 v10, 7, v4
	v_sub_u32_e32 v12, v12, v13
	v_add_u32_e32 v13, s44, v9
	v_mad_i64_i32 v[16:17], s[28:29], v13, s33, v[2:3]
	v_lshlrev_b32_e32 v2, 3, v12
	v_ashrrev_i32_e32 v117, 3, v118
	v_lshlrev_b32_e32 v30, 4, v10
	v_ashrrev_i32_e32 v3, 31, v2
	v_add_u32_e32 v13, s44, v117
	v_lshl_add_u64 v[120:121], s[42:43], 0, v[30:31]
	v_lshl_add_u64 v[16:17], v[2:3], 1, v[16:17]
	global_load_dwordx4 v[96:99], v[14:15], off offset:3392
	global_load_dwordx4 v[100:103], v[16:17], off offset:3392
	v_mad_i64_i32 v[14:15], s[28:29], v13, s33, v[120:121]
	v_add_u32_e32 v13, 64, v13
	v_mad_i64_i32 v[16:17], s[28:29], v13, s33, v[120:121]
	global_load_dwordx4 v[104:107], v[14:15], off offset:3648
	global_load_dwordx4 v[108:111], v[16:17], off offset:3648
	s_movk_i32 s28, 0x80
	v_cmp_gt_i32_e64 s[40:41], s28, v118
	v_mov_b32_e32 v158, 0
	s_and_saveexec_b64 s[46:47], s[40:41]
	s_cbranch_execz .LBB0_1032
	v_add_u32_e32 v14, s44, v118
	v_ashrrev_i32_e32 v15, 31, v14
	v_lshl_add_u64 v[14:15], v[14:15], 2, s[6:7]
	global_load_dword v13, v[14:15], off
	s_waitcnt vmcnt(0)
	v_sub_u32_e32 v13, v13, v115
	v_cvt_f32_i32_e32 v158, v13
